# cb3: in3 + MoE combine: the wave's four tokens' (expert, position, weight) records fetched together instead of in a dependent ladder
# speedup vs baseline: 1.0049x; 1.0049x over previous
; template <int NTK>
; __device__ __forceinline__ void combine_rows(int t0, int tstride, const LAS int* bst, const int* tok_e, const int* tok_pos, const float* tok_w, const bf16_t* Y, const bf16_t* xbi, float* xio, bf16_t* xb, float* part, const float* gfin, bool last, int lane) {
;     ...
;     for (int i = 0; i < NTK; ++i) { const int t = t0 + i * tstride; ok[i] = t < T; tk[i] = ok[i] ? t : T - 1; }
; #pragma unroll
;     for (int i = 0; i < NTK; ++i) { const int t = tk[i]; const int e0 = tok_e[2 * t], e1 = tok_e[2 * t + 1]; w0[i] = tok_w[2 * t]; w1[i] = tok_w[2 * t + 1];
;         s0[i] = (size_t)bst[e0] * 256 + tok_pos[2 * t]; s1[i] = (size_t)bst[e1] * 256 + tok_pos[2 * t + 1]; }
.LBB0_1633:
	s_add_i32 s6, s54, s12
	s_cmpk_lt_i32 s6, 0x4000
	s_cselect_b64 s[28:29], -1, 0
	s_and_b64 s[2:3], s[28:29], exec
	v_readlane_b32 s2, v252, 24
	s_cselect_b32 s26, s6, 0x3fff
	s_add_i32 s6, s2, s12
	s_cmpk_lt_i32 s6, 0x4000
	s_cselect_b64 s[24:25], -1, 0
	s_and_b64 s[2:3], s[24:25], exec
	v_readlane_b32 s2, v251, 2
	s_mul_i32 s2, s2, 24
	s_cselect_b32 s22, s6, 0x3fff
	s_add_i32 s6, s2, s12
	s_cmpk_lt_i32 s6, 0x4000
	s_cselect_b64 s[20:21], -1, 0
	s_and_b64 s[2:3], s[20:21], exec
	s_cselect_b32 s18, s6, 0x3fff
	s_ashr_i32 s17, s16, 31
	s_lshl_b64 s[6:7], s[16:17], 2
	v_readlane_b32 s10, v251, 34
	v_readlane_b32 s11, v251, 35
	s_add_u32 s2, s10, s6
	s_addc_u32 s3, s11, s7
	global_load_dwordx2 v[14:15], v161, s[2:3]
	s_add_i32 s2, s16, 1
	s_ashr_i32 s3, s2, 31
	v_readlane_b32 s34, v251, 38
	v_readlane_b32 s35, v251, 39
	s_add_u32 s8, s34, s6
	s_addc_u32 s9, s35, s7
	global_load_dword v82, v161, s[8:9]
	s_lshl_b64 s[8:9], s[2:3], 2
	s_add_u32 s2, s34, s8
	s_addc_u32 s3, s35, s9
	global_load_dword v84, v161, s[2:3]
	s_add_i32 s2, 0, 0x23900
	v_readlane_b32 s30, v251, 36
	v_readlane_b32 s31, v251, 37
	s_add_u32 s6, s30, s6
	s_addc_u32 s7, s31, s7
	global_load_dword v44, v161, s[6:7]
	s_add_u32 s6, s30, s8
	s_addc_u32 s7, s31, s9
	global_load_dword v46, v161, s[6:7]
	s_lshl_b32 s6, s26, 1
	s_ashr_i32 s7, s6, 31
	s_lshl_b64 s[6:7], s[6:7], 2
	s_add_u32 s8, s10, s6
	s_addc_u32 s9, s11, s7
	s_lshl_b32 s6, s26, 1
	s_ashr_i32 s7, s6, 31
	s_lshl_b64 s[6:7], s[6:7], 2
	s_add_u32 s8, s10, s6
	s_addc_u32 s9, s11, s7
	global_load_dwordx2 v[142:143], v161, s[8:9]
	s_add_u32 s8, s34, s6
	s_addc_u32 s9, s35, s7
	global_load_dwordx2 v[64:65], v161, s[8:9]
	s_add_u32 s8, s30, s6
	s_addc_u32 s9, s31, s7
	global_load_dwordx2 v[16:17], v161, s[8:9]
	s_lshl_b32 s6, s22, 1
	s_ashr_i32 s7, s6, 31
	s_lshl_b64 s[6:7], s[6:7], 2
	s_add_u32 s8, s10, s6
	s_addc_u32 s9, s11, s7
	global_load_dwordx2 v[144:145], v161, s[8:9]
	s_add_u32 s8, s34, s6
	s_addc_u32 s9, s35, s7
	global_load_dwordx2 v[146:147], v161, s[8:9]
	s_add_u32 s8, s30, s6
	s_addc_u32 s9, s31, s7
	global_load_dwordx2 v[18:19], v161, s[8:9]
	s_lshl_b32 s6, s18, 1
	s_ashr_i32 s7, s6, 31
	s_lshl_b64 s[6:7], s[6:7], 2
	s_add_u32 s8, s10, s6
	s_addc_u32 s9, s11, s7
	global_load_dwordx2 v[148:149], v161, s[8:9]
	s_add_u32 s8, s34, s6
	s_addc_u32 s9, s35, s7
	global_load_dwordx2 v[150:151], v161, s[8:9]
	s_add_u32 s8, s30, s6
	s_addc_u32 s9, s31, s7
	global_load_dwordx2 v[48:49], v161, s[8:9]
	v_lshl_add_u64 v[102:103], s[52:53], 0, v[8:9]
	s_waitcnt vmcnt(0)
	v_lshlrev_b32_e32 v14, 2, v14
	v_add_u32_e32 v14, s2, v14
	ds_read_b32 v38, v14
	v_lshlrev_b32_e32 v14, 2, v15
	v_add_u32_e32 v14, s2, v14
	ds_read_b32 v42, v14
	s_add_u32 s8, s34, s6
	s_addc_u32 s9, s35, s7
	s_add_u32 s6, s30, s6
	s_addc_u32 s7, s31, s7
	s_lshl_b32 s6, s22, 1
	s_ashr_i32 s7, s6, 31
	s_lshl_b64 s[6:7], s[6:7], 2
	s_add_u32 s8, s10, s6
	s_addc_u32 s9, s11, s7
	s_waitcnt lgkmcnt(1)
	v_ashrrev_i32_e32 v39, 31, v38
	v_ashrrev_i32_e32 v45, 31, v44
	s_waitcnt lgkmcnt(0)
	v_ashrrev_i32_e32 v43, 31, v42
	v_lshlrev_b64 v[38:39], 19, v[38:39]
	v_ashrrev_i32_e32 v47, 31, v46
	v_lshlrev_b64 v[44:45], 11, v[44:45]
	v_lshlrev_b64 v[42:43], 19, v[42:43]
	s_waitcnt vmcnt(2)
	v_lshlrev_b32_e32 v14, 2, v142
	v_add_u32_e32 v14, s2, v14
	ds_read_b32 v20, v14
	v_lshlrev_b32_e32 v14, 2, v143
	v_add_u32_e32 v14, s2, v14
	ds_read_b32 v26, v14
	s_add_u32 s8, s34, s6
	s_addc_u32 s9, s35, s7
	s_add_u32 s6, s30, s6
	s_addc_u32 s7, s31, s7
	s_waitcnt vmcnt(1)
	v_ashrrev_i32_e32 v25, 31, v16
	v_mov_b32_e32 v24, v16
	v_ashrrev_i32_e32 v29, 31, v17
	v_mov_b32_e32 v28, v17
	s_lshl_b32 s6, s18, 1
	s_ashr_i32 s7, s6, 31
	s_lshl_b64 s[6:7], s[6:7], 2
	s_add_u32 s8, s10, s6
	s_addc_u32 s9, s11, s7
	s_waitcnt lgkmcnt(1)
	v_ashrrev_i32_e32 v21, 31, v20
	v_lshlrev_b64 v[20:21], 19, v[20:21]
	s_waitcnt lgkmcnt(0)
	v_ashrrev_i32_e32 v27, 31, v26
	v_lshlrev_b64 v[24:25], 11, v[24:25]
	s_waitcnt vmcnt(2)
	v_lshlrev_b32_e32 v14, 2, v144
	v_add_u32_e32 v14, s2, v14
	ds_read_b32 v30, v14
	s_waitcnt vmcnt(0)
	v_ashrrev_i32_e32 v33, 31, v18
	v_mov_b32_e32 v32, v18
	v_ashrrev_i32_e32 v37, 31, v19
	v_mov_b32_e32 v36, v19
	s_add_u32 s8, s34, s6
	s_addc_u32 s9, s35, s7
	s_add_u32 s6, s30, s6
	s_addc_u32 s7, s31, s7
	s_ashr_i32 s27, s26, 31
	s_ashr_i32 s23, s22, 31
	s_ashr_i32 s19, s18, 31
	s_waitcnt vmcnt(1)
	v_lshlrev_b32_e32 v18, 2, v148
	v_add_u32_e32 v18, s2, v18
	ds_read_b32 v40, v18
	v_lshlrev_b32_e32 v14, 2, v145
	v_lshlrev_b32_e32 v18, 2, v149
	v_add_u32_e32 v14, s2, v14
	v_add_u32_e32 v18, s2, v18
	ds_read_b32 v34, v14
	ds_read_b32 v18, v18
	v_readlane_b32 s8, v251, 56
	v_readlane_b32 s9, v251, 57
	s_mov_b32 s2, 0x2a00000
	s_waitcnt lgkmcnt(3)
	v_ashrrev_i32_e32 v31, 31, v30
	v_lshl_add_u64 v[38:39], s[8:9], 0, v[38:39]
	v_lshl_add_u64 v[38:39], v[38:39], 0, v[44:45]
	v_lshlrev_b64 v[44:45], 11, v[46:47]
	v_lshl_add_u64 v[42:43], s[8:9], 0, v[42:43]
	v_lshl_add_u64 v[42:43], v[42:43], 0, v[44:45]
	v_add_co_u32_e32 v44, vcc, s2, v102
	v_readfirstlane_b32 s6, v38
	s_nop 0
	v_addc_co_u32_e32 v45, vcc, 0, v103, vcc
	v_readfirstlane_b32 s7, v39
	v_readfirstlane_b32 s10, v42
	v_readfirstlane_b32 s11, v43
	global_load_dwordx2 v[46:47], v[44:45], off
	v_lshl_add_u64 v[20:21], s[8:9], 0, v[20:21]
	v_lshl_add_u64 v[20:21], v[20:21], 0, v[24:25]
	global_load_dwordx2 v[110:111], v140, s[6:7]
	s_nop 0
	global_load_dwordx2 v[108:109], v140, s[10:11]
	global_load_dwordx2 v[38:39], v[44:45], off offset:512
	v_lshlrev_b64 v[24:25], 19, v[26:27]
	s_lshl_b64 s[2:3], s[26:27], 11
	v_lshlrev_b64 v[26:27], 11, v[28:29]
	v_lshl_add_u64 v[24:25], s[8:9], 0, v[24:25]
	v_lshl_add_u64 v[24:25], v[24:25], 0, v[26:27]
	v_lshl_add_u64 v[72:73], v[4:5], 0, s[2:3]
	v_readfirstlane_b32 s2, v20
	v_readfirstlane_b32 s3, v21
	v_lshlrev_b64 v[20:21], 19, v[30:31]
	s_waitcnt lgkmcnt(1)
; __device__ __forceinline__ float bf_lo(unsigned w) { return __uint_as_float(w << 16); }
; __device__ __forceinline__ float bf_hi(unsigned w) { return __uint_as_float(w & 0xffff0000u); }
; __device__ __forceinline__ f32x4 ld_bf4(const bf16_t* p) { const u32x2 w = *(const u32x2*)p; return (f32x4){bf_lo(w.x), bf_hi(w.x), bf_lo(w.y), bf_hi(w.y)}; }
; template <int NTK>
; __device__ __forceinline__ void combine_rows(int t0, int tstride, const LAS int* bst, const int* tok_e, const int* tok_pos, const float* tok_w, const bf16_t* Y, const bf16_t* xbi, float* xio, bf16_t* xb, float* part, const float* gfin, bool last, int lane) {
;     ...
;     for (int i = 0; i < NTK; ++i)
; #pragma unroll
;         for (int j = 0; j < 4; ++j) { const int c = j * 256 + lane * 4; v[i][j] = ld_bf4(xbi + (size_t)tk[i] * DM + c); ya[i][j] = *(const u32x2*)(Y + s0[i] * DM + c); yb[i][j] = *(const u32x2*)(Y + s1[i] * DM + c); }
; #pragma unroll
;     for (int i = 0; i < NTK; ++i) { float s = 0.f;
; #pragma unroll
;         for (int j = 0; j < 4; ++j) { const f32x4 a = {bf_lo(ya[i][j].x), bf_hi(ya[i][j].x), bf_lo(ya[i][j].y), bf_hi(ya[i][j].y)}, b = {bf_lo(yb[i][j].x), bf_hi(yb[i][j].x), bf_lo(yb[i][j].y), bf_hi(yb[i][j].y)};
;             v[i][j] = v[i][j] + w0[i] * a + w1[i] * b;
;             s += (v[i][j][0] * v[i][j][0] + v[i][j][1] * v[i][j][1]) + (v[i][j][2] * v[i][j][2] + v[i][j][3] * v[i][j][3]); }
	v_ashrrev_i32_e32 v35, 31, v34
	v_lshl_add_u64 v[20:21], s[8:9], 0, v[20:21]
	v_ashrrev_i32_e32 v41, 31, v40
	s_waitcnt lgkmcnt(0)
	v_ashrrev_i32_e32 v19, 31, v18
	v_lshlrev_b64 v[26:27], 11, v[36:37]
	v_lshlrev_b64 v[18:19], 19, v[18:19]
	v_lshl_add_u64 v[18:19], s[8:9], 0, v[18:19]
	s_andn2_b64 vcc, exec, s[14:15]
	s_waitcnt vmcnt(5)
	v_ashrrev_i32_e32 v67, 31, v48
	v_mov_b32_e32 v66, v48
	v_ashrrev_i32_e32 v23, 31, v49
	v_mov_b32_e32 v22, v49
	v_lshlrev_b64 v[22:23], 11, v[22:23]
	v_lshl_add_u64 v[22:23], v[18:19], 0, v[22:23]
	s_waitcnt vmcnt(3)
	v_lshlrev_b32_e32 v106, 16, v46
	v_and_b32_e32 v107, 0xffff0000, v46
	v_lshlrev_b32_e32 v104, 16, v47
	v_and_b32_e32 v105, 0xffff0000, v47
	s_waitcnt vmcnt(0)
	v_lshlrev_b32_e32 v118, 16, v38
	v_and_b32_e32 v119, 0xffff0000, v38
	v_lshlrev_b32_e32 v114, 16, v39
	v_and_b32_e32 v115, 0xffff0000, v39
	global_load_dwordx2 v[130:131], v140, s[6:7] offset:512
	global_load_dwordx2 v[126:127], v140, s[10:11] offset:512
	global_load_dwordx2 v[38:39], v[44:45], off offset:1024
	v_lshlrev_b32_e32 v136, 16, v110
	v_and_b32_e32 v137, 0xffff0000, v110
	v_lshlrev_b32_e32 v110, 16, v111
	v_and_b32_e32 v111, 0xffff0000, v111
	v_lshlrev_b32_e32 v138, 16, v108
	v_and_b32_e32 v139, 0xffff0000, v108
	v_lshlrev_b32_e32 v108, 16, v109
	v_and_b32_e32 v109, 0xffff0000, v109
	v_pk_fma_f32 v[106:107], v[82:83], v[136:137], v[106:107] op_sel_hi:[0,1,1]
	v_pk_fma_f32 v[104:105], v[82:83], v[110:111], v[104:105] op_sel_hi:[0,1,1]
	v_pk_fma_f32 v[136:137], v[84:85], v[108:109], v[104:105] op_sel_hi:[0,1,1]
	v_pk_fma_f32 v[138:139], v[84:85], v[138:139], v[106:107] op_sel_hi:[0,1,1]
	v_mul_f32_e32 v83, v139, v139
	v_mul_f32_e32 v85, v137, v137
	v_fmac_f32_e32 v83, v138, v138
	v_fmac_f32_e32 v85, v136, v136
	v_add_f32_e32 v83, v83, v85
	s_waitcnt vmcnt(2)
	v_lshlrev_b32_e32 v104, 16, v130
	v_and_b32_e32 v105, 0xffff0000, v130
	s_waitcnt vmcnt(0)
	v_lshlrev_b32_e32 v116, 16, v38
	v_and_b32_e32 v117, 0xffff0000, v38
	v_lshlrev_b32_e32 v112, 16, v39
	v_and_b32_e32 v113, 0xffff0000, v39
	global_load_dwordx2 v[128:129], v140, s[6:7] offset:1024
	global_load_dwordx2 v[124:125], v140, s[10:11] offset:1024
	global_load_dwordx2 v[38:39], v[44:45], off offset:1536
	global_load_dwordx2 v[134:135], v140, s[6:7] offset:1536
	global_load_dwordx2 v[132:133], v140, s[10:11] offset:1536
	v_readfirstlane_b32 s6, v24
	v_readfirstlane_b32 s7, v25
	v_lshlrev_b64 v[24:25], 11, v[32:33]
	v_lshl_add_u64 v[24:25], v[20:21], 0, v[24:25]
	v_lshlrev_b64 v[20:21], 19, v[34:35]
	global_load_dwordx2 v[94:95], v[72:73], off
	global_load_dwordx2 v[92:93], v140, s[2:3]
	global_load_dwordx2 v[90:91], v140, s[6:7]
	global_load_dwordx2 v[100:101], v[72:73], off offset:512
	global_load_dwordx2 v[88:89], v140, s[2:3] offset:512
	global_load_dwordx2 v[86:87], v140, s[6:7] offset:512
	global_load_dwordx2 v[98:99], v[72:73], off offset:1024
	global_load_dwordx2 v[80:81], v140, s[2:3] offset:1024
	global_load_dwordx2 v[78:79], v140, s[6:7] offset:1024
	global_load_dwordx2 v[96:97], v[72:73], off offset:1536
	global_load_dwordx2 v[76:77], v140, s[2:3] offset:1536
	global_load_dwordx2 v[74:75], v140, s[6:7] offset:1536
	s_lshl_b64 s[2:3], s[22:23], 11
	v_lshl_add_u64 v[20:21], s[8:9], 0, v[20:21]
	v_lshl_add_u64 v[26:27], v[20:21], 0, v[26:27]
	v_lshl_add_u64 v[20:21], v[4:5], 0, s[2:3]
	v_readfirstlane_b32 s2, v24
	v_readfirstlane_b32 s3, v25
	v_lshlrev_b64 v[24:25], 19, v[40:41]
	v_readfirstlane_b32 s6, v26
	v_readfirstlane_b32 s7, v27
	v_lshlrev_b64 v[26:27], 11, v[66:67]
	v_lshl_add_u64 v[24:25], s[8:9], 0, v[24:25]
	global_load_dwordx2 v[56:57], v[20:21], off
	global_load_dwordx2 v[54:55], v140, s[2:3]
	v_lshl_add_u64 v[24:25], v[24:25], 0, v[26:27]
	v_readfirstlane_b32 s10, v22
	v_readfirstlane_b32 s11, v23
	v_lshlrev_b32_e32 v106, 16, v131
	v_and_b32_e32 v107, 0xffff0000, v131
	v_lshlrev_b32_e32 v108, 16, v126
	v_and_b32_e32 v109, 0xffff0000, v126
	v_lshlrev_b32_e32 v110, 16, v127
	v_and_b32_e32 v111, 0xffff0000, v127
	v_pk_fma_f32 v[118:119], v[82:83], v[104:105], v[118:119] op_sel_hi:[0,1,1]
	v_pk_fma_f32 v[104:105], v[82:83], v[106:107], v[114:115] op_sel_hi:[0,1,1]
	v_pk_fma_f32 v[104:105], v[84:85], v[110:111], v[104:105] op_sel_hi:[0,1,1]
	v_pk_fma_f32 v[108:109], v[84:85], v[108:109], v[118:119] op_sel_hi:[0,1,1]
	v_mul_f32_e32 v85, v109, v109
	v_mul_f32_e32 v106, v105, v105
	v_fmac_f32_e32 v85, v108, v108
	v_fmac_f32_e32 v106, v104, v104
	v_add_f32_e32 v85, v85, v106
	v_add_f32_e32 v83, v83, v85
	s_waitcnt vmcnt(18)
	v_lshlrev_b32_e32 v106, 16, v128
	v_and_b32_e32 v107, 0xffff0000, v128
	s_waitcnt vmcnt(16)
; __device__ __forceinline__ float bf_lo(unsigned w) { return __uint_as_float(w << 16); }
; __device__ __forceinline__ float bf_hi(unsigned w) { return __uint_as_float(w & 0xffff0000u); }
; __device__ __forceinline__ float wave_sum(float v) { return half_sum(sum32(v)); }
; __device__ __forceinline__ f32x4 ld_bf4(const bf16_t* p) { const u32x2 w = *(const u32x2*)p; return (f32x4){bf_lo(w.x), bf_hi(w.x), bf_lo(w.y), bf_hi(w.y)}; }
; __device__ __forceinline__ void st_bf4(bf16_t* p, f32x4 v) { u32x2 w; w.x = cvt_pk_bf16(v[0], v[1]); w.y = cvt_pk_bf16(v[2], v[3]); *(u32x2*)p = w; }
; template <int NTK>
; __device__ __forceinline__ void combine_rows(int t0, int tstride, const LAS int* bst, const int* tok_e, const int* tok_pos, const float* tok_w, const bf16_t* Y, const bf16_t* xbi, float* xio, bf16_t* xb, float* part, const float* gfin, bool last, int lane) {
;     ...
;     for (int i = 0; i < NTK; ++i)
; #pragma unroll
;         for (int j = 0; j < 4; ++j) { const int c = j * 256 + lane * 4; v[i][j] = ld_bf4(xbi + (size_t)tk[i] * DM + c); ya[i][j] = *(const u32x2*)(Y + s0[i] * DM + c); yb[i][j] = *(const u32x2*)(Y + s1[i] * DM + c); }
; #pragma unroll
;     for (int i = 0; i < NTK; ++i) { float s = 0.f;
; #pragma unroll
;         for (int j = 0; j < 4; ++j) { const f32x4 a = {bf_lo(ya[i][j].x), bf_hi(ya[i][j].x), bf_lo(ya[i][j].y), bf_hi(ya[i][j].y)}, b = {bf_lo(yb[i][j].x), bf_hi(yb[i][j].x), bf_lo(yb[i][j].y), bf_hi(yb[i][j].y)};
;             v[i][j] = v[i][j] + w0[i] * a + w1[i] * b;
;             s += (v[i][j][0] * v[i][j][0] + v[i][j][1] * v[i][j][1]) + (v[i][j][2] * v[i][j][2] + v[i][j][3] * v[i][j][3]); }
;         s = wave_sum(s);
;         if (ok[i]) { const int t = tk[i];
;             if (!last) {
; #pragma unroll
;                 for (int j = 0; j < 4; ++j) { const int c = j * 256 + lane * 4; st_bf4(xb + (size_t)t * DM + c, v[i][j]); }
;                 if (lane < 16) part[(size_t)t * 16 + lane] = lane == 0 ? s : 0.f;
	v_lshlrev_b32_e32 v122, 16, v38
	v_and_b32_e32 v123, 0xffff0000, v38
	v_lshlrev_b32_e32 v120, 16, v39
	v_and_b32_e32 v121, 0xffff0000, v39
	global_load_dwordx2 v[52:53], v140, s[6:7]
	global_load_dwordx2 v[62:63], v[20:21], off offset:512
	global_load_dwordx2 v[50:51], v140, s[2:3] offset:512
	global_load_dwordx2 v[48:49], v140, s[6:7] offset:512
	global_load_dwordx2 v[60:61], v[20:21], off offset:1024
	global_load_dwordx2 v[46:47], v140, s[2:3] offset:1024
	global_load_dwordx2 v[44:45], v140, s[6:7] offset:1024
	global_load_dwordx2 v[58:59], v[20:21], off offset:1536
	global_load_dwordx2 v[38:39], v140, s[2:3] offset:1536
	global_load_dwordx2 v[36:37], v140, s[6:7] offset:1536
	s_lshl_b64 s[6:7], s[18:19], 11
	v_lshl_add_u64 v[18:19], v[4:5], 0, s[6:7]
	v_readfirstlane_b32 s6, v24
	v_readfirstlane_b32 s7, v25
	global_load_dwordx2 v[32:33], v[18:19], off
	v_lshlrev_b32_e32 v110, 16, v129
	v_and_b32_e32 v111, 0xffff0000, v129
	v_lshlrev_b32_e32 v114, 16, v124
	v_and_b32_e32 v115, 0xffff0000, v124
	global_load_dwordx2 v[30:31], v140, s[6:7]
	global_load_dwordx2 v[34:35], v140, s[10:11]
	global_load_dwordx2 v[40:41], v[18:19], off offset:512
	global_load_dwordx2 v[26:27], v140, s[6:7] offset:512
	global_load_dwordx2 v[28:29], v140, s[10:11] offset:512
	global_load_dwordx2 v[42:43], v[18:19], off offset:1024
	global_load_dwordx2 v[22:23], v140, s[6:7] offset:1024
	global_load_dwordx2 v[24:25], v140, s[10:11] offset:1024
	global_load_dwordx2 v[70:71], v[18:19], off offset:1536
	global_load_dwordx2 v[66:67], v140, s[6:7] offset:1536
	global_load_dwordx2 v[68:69], v140, s[10:11] offset:1536
	v_lshlrev_b32_e32 v118, 16, v125
	v_and_b32_e32 v119, 0xffff0000, v125
	v_pk_fma_f32 v[116:117], v[82:83], v[106:107], v[116:117] op_sel_hi:[0,1,1]
	v_pk_fma_f32 v[106:107], v[82:83], v[110:111], v[112:113] op_sel_hi:[0,1,1]
	v_pk_fma_f32 v[106:107], v[84:85], v[118:119], v[106:107] op_sel_hi:[0,1,1]
	v_pk_fma_f32 v[110:111], v[84:85], v[114:115], v[116:117] op_sel_hi:[0,1,1]
	v_mul_f32_e32 v85, v111, v111
	v_mul_f32_e32 v112, v107, v107
	v_fmac_f32_e32 v85, v110, v110
	v_fmac_f32_e32 v112, v106, v106
	v_add_f32_e32 v85, v85, v112
	s_waitcnt vmcnt(37)
	v_lshlrev_b32_e32 v112, 16, v134
	v_and_b32_e32 v113, 0xffff0000, v134
	v_lshlrev_b32_e32 v114, 16, v135
	v_and_b32_e32 v115, 0xffff0000, v135
	v_add_f32_e32 v124, v83, v85
	s_waitcnt vmcnt(36)
	v_lshlrev_b32_e32 v116, 16, v132
	v_and_b32_e32 v117, 0xffff0000, v132
	v_lshlrev_b32_e32 v118, 16, v133
	v_and_b32_e32 v119, 0xffff0000, v133
	v_pk_fma_f32 v[112:113], v[82:83], v[112:113], v[122:123] op_sel_hi:[0,1,1]
	v_pk_fma_f32 v[82:83], v[82:83], v[114:115], v[120:121] op_sel_hi:[0,1,1]
	v_pk_fma_f32 v[82:83], v[84:85], v[118:119], v[82:83] op_sel_hi:[0,1,1]
	v_pk_fma_f32 v[84:85], v[84:85], v[116:117], v[112:113] op_sel_hi:[0,1,1]
	v_mul_f32_e32 v112, v85, v85
	v_mul_f32_e32 v113, v83, v83
	v_fmac_f32_e32 v112, v84, v84
	v_fmac_f32_e32 v113, v82, v82
	v_add_f32_e32 v112, v112, v113
	v_add_f32_e32 v112, v124, v112
	s_mov_b64 s[10:11], -1
	s_waitcnt lgkmcnt(0)
	s_nop 1
	v_add_f32_dpp v112, v112, v112 quad_perm:[1,0,3,2] row_mask:0xf bank_mask:0xf
	s_waitcnt lgkmcnt(0)
	s_nop 1
	v_add_f32_dpp v112, v112, v112 quad_perm:[2,3,0,1] row_mask:0xf bank_mask:0xf
	s_waitcnt lgkmcnt(0)
	s_nop 1
	v_add_f32_dpp v112, v112, v112 row_half_mirror row_mask:0xf bank_mask:0xf
	s_waitcnt lgkmcnt(0)
	s_nop 1
	v_add_f32_dpp v112, v112, v112 row_mirror row_mask:0xf bank_mask:0xf
	v_mov_b32_e32 v113, v112
	s_waitcnt lgkmcnt(0)
	s_nop 1
	v_permlane16_swap_b32_e32 v113, v112
	v_add_f32_e32 v112, v112, v113
	v_mov_b32_e32 v113, v112
	s_nop 1
	v_permlane32_swap_b32_e32 v112, v113
	v_add_f32_e32 v112, v112, v113
	v_cndmask_b32_e64 v113, 0, 1, s[14:15]
	v_cmp_ne_u32_e64 s[6:7], 1, v113
	s_cbranch_vccnz .LBB0_1637
	s_mov_b64 s[2:3], 0x2a00000
	v_lshl_add_u64 v[114:115], v[102:103], 0, s[2:3]
	s_mov_b64 s[2:3], 0x2a00200
	v_lshl_add_u64 v[116:117], v[102:103], 0, s[2:3]
	s_mov_b64 s[2:3], 0x2a00400
	v_lshl_add_u64 v[118:119], v[102:103], 0, s[2:3]
	s_mov_b64 s[2:3], 0x2a00600
	v_cvt_pk_bf16_f32 v120, v138, v139
	v_cvt_pk_bf16_f32 v121, v136, v137
	global_store_dwordx2 v[114:115], v[120:121], off
	v_cvt_pk_bf16_f32 v114, v108, v109
	v_cvt_pk_bf16_f32 v115, v104, v105
	v_lshl_add_u64 v[102:103], v[102:103], 0, s[2:3]
	global_store_dwordx2 v[116:117], v[114:115], off
	v_cvt_pk_bf16_f32 v114, v110, v111
	v_cvt_pk_bf16_f32 v115, v106, v107
	global_store_dwordx2 v[118:119], v[114:115], off
	v_cvt_pk_bf16_f32 v114, v84, v85
	v_cvt_pk_bf16_f32 v115, v82, v83
	global_store_dwordx2 v[102:103], v[114:115], off
	s_and_saveexec_b64 s[10:11], s[0:1]
	s_cbranch_execz .LBB0_1636
	v_cndmask_b32_e64 v113, 0, v112, s[4:5]
	v_lshl_add_u64 v[102:103], s[52:53], 0, v[12:13]
	global_store_dword v[102:103], v113, off

; __device__ __forceinline__ float bf_lo(unsigned w) { return __uint_as_float(w << 16); }
; __device__ __forceinline__ float bf_hi(unsigned w) { return __uint_as_float(w & 0xffff0000u); }
; __device__ __forceinline__ float wave_sum(float v) { return half_sum(sum32(v)); }
; __device__ __forceinline__ void st_bf4(bf16_t* p, f32x4 v) { u32x2 w; w.x = cvt_pk_bf16(v[0], v[1]); w.y = cvt_pk_bf16(v[2], v[3]); *(u32x2*)p = w; }
; template <int NTK>
; __device__ __forceinline__ void combine_rows(int t0, int tstride, const LAS int* bst, const int* tok_e, const int* tok_pos, const float* tok_w, const bf16_t* Y, const bf16_t* xbi, float* xio, bf16_t* xb, float* part, const float* gfin, bool last, int lane) {
;     ...
;     for (int i = 0; i < NTK; ++i) { float s = 0.f;
; #pragma unroll
;         for (int j = 0; j < 4; ++j) { const f32x4 a = {bf_lo(ya[i][j].x), bf_hi(ya[i][j].x), bf_lo(ya[i][j].y), bf_hi(ya[i][j].y)}, b = {bf_lo(yb[i][j].x), bf_hi(yb[i][j].x), bf_lo(yb[i][j].y), bf_hi(yb[i][j].y)};
;             v[i][j] = v[i][j] + w0[i] * a + w1[i] * b;
;             s += (v[i][j][0] * v[i][j][0] + v[i][j][1] * v[i][j][1]) + (v[i][j][2] * v[i][j][2] + v[i][j][3] * v[i][j][3]); }
;         s = wave_sum(s);
;         if (ok[i]) { const int t = tk[i];
;             if (!last) {
; #pragma unroll
;                 for (int j = 0; j < 4; ++j) { const int c = j * 256 + lane * 4; st_bf4(xb + (size_t)t * DM + c, v[i][j]); }
;                 if (lane < 16) part[(size_t)t * 16 + lane] = lane == 0 ? s : 0.f;
.LBB0_1646:
	s_waitcnt vmcnt(23)
	v_lshlrev_b32_e32 v64, 16, v56
	v_and_b32_e32 v65, 0xffff0000, v56
	v_lshlrev_b32_e32 v56, 16, v57
	v_and_b32_e32 v57, 0xffff0000, v57
	s_waitcnt vmcnt(22)
	v_lshlrev_b32_e32 v78, 16, v54
	v_and_b32_e32 v79, 0xffff0000, v54
	v_lshlrev_b32_e32 v54, 16, v55
	v_and_b32_e32 v55, 0xffff0000, v55
	s_waitcnt vmcnt(21)
	v_lshlrev_b32_e32 v80, 16, v52
	v_and_b32_e32 v81, 0xffff0000, v52
	v_lshlrev_b32_e32 v52, 16, v53
	v_and_b32_e32 v53, 0xffff0000, v53
	v_pk_fma_f32 v[64:65], v[146:147], v[78:79], v[64:65] op_sel_hi:[0,1,1]
	v_pk_fma_f32 v[54:55], v[146:147], v[54:55], v[56:57] op_sel_hi:[0,1,1]
	v_pk_fma_f32 v[52:53], v[146:147], v[52:53], v[54:55] op_sel:[1,0,0]
	v_pk_fma_f32 v[54:55], v[146:147], v[80:81], v[64:65] op_sel:[1,0,0]
	v_mul_f32_e32 v57, v53, v53
	v_mul_f32_e32 v56, v55, v55
	v_fmac_f32_e32 v56, v54, v54
	v_fmac_f32_e32 v57, v52, v52
	s_waitcnt vmcnt(20)
	v_lshlrev_b32_e32 v72, 16, v62
	v_and_b32_e32 v73, 0xffff0000, v62
	v_lshlrev_b32_e32 v62, 16, v63
	v_and_b32_e32 v63, 0xffff0000, v63
	v_add_f32_e32 v78, v56, v57
	s_waitcnt vmcnt(19)
	v_lshlrev_b32_e32 v56, 16, v50
	v_and_b32_e32 v57, 0xffff0000, v50
	v_lshlrev_b32_e32 v50, 16, v51
	v_and_b32_e32 v51, 0xffff0000, v51
	s_waitcnt vmcnt(18)
	v_lshlrev_b32_e32 v64, 16, v48
	v_and_b32_e32 v65, 0xffff0000, v48
	v_lshlrev_b32_e32 v48, 16, v49
	v_and_b32_e32 v49, 0xffff0000, v49
	v_pk_fma_f32 v[56:57], v[146:147], v[56:57], v[72:73] op_sel_hi:[0,1,1]
	v_pk_fma_f32 v[50:51], v[146:147], v[50:51], v[62:63] op_sel_hi:[0,1,1]
	v_pk_fma_f32 v[48:49], v[146:147], v[48:49], v[50:51] op_sel:[1,0,0]
	v_pk_fma_f32 v[50:51], v[146:147], v[64:65], v[56:57] op_sel:[1,0,0]
	v_mul_f32_e32 v57, v49, v49
	v_mul_f32_e32 v56, v51, v51
	v_fmac_f32_e32 v56, v50, v50
	v_fmac_f32_e32 v57, v48, v48
	v_add_f32_e32 v56, v56, v57
	s_waitcnt vmcnt(17)
	v_lshlrev_b32_e32 v74, 16, v60
	v_and_b32_e32 v75, 0xffff0000, v60
	v_lshlrev_b32_e32 v60, 16, v61
	v_and_b32_e32 v61, 0xffff0000, v61
	v_add_f32_e32 v64, v78, v56
	s_waitcnt vmcnt(16)
	v_lshlrev_b32_e32 v56, 16, v46
	v_and_b32_e32 v57, 0xffff0000, v46
	v_lshlrev_b32_e32 v46, 16, v47
	v_and_b32_e32 v47, 0xffff0000, v47
	s_waitcnt vmcnt(15)
	v_lshlrev_b32_e32 v62, 16, v44
	v_and_b32_e32 v63, 0xffff0000, v44
	v_lshlrev_b32_e32 v44, 16, v45
	v_and_b32_e32 v45, 0xffff0000, v45
	v_pk_fma_f32 v[56:57], v[146:147], v[56:57], v[74:75] op_sel_hi:[0,1,1]
	v_pk_fma_f32 v[46:47], v[146:147], v[46:47], v[60:61] op_sel_hi:[0,1,1]
	v_pk_fma_f32 v[44:45], v[146:147], v[44:45], v[46:47] op_sel:[1,0,0]
	v_pk_fma_f32 v[46:47], v[146:147], v[62:63], v[56:57] op_sel:[1,0,0]
	v_mul_f32_e32 v57, v45, v45
	v_mul_f32_e32 v56, v47, v47
	v_fmac_f32_e32 v56, v46, v46
	v_fmac_f32_e32 v57, v44, v44
	v_add_f32_e32 v56, v56, v57
	s_waitcnt vmcnt(14)
	v_lshlrev_b32_e32 v76, 16, v58
	v_and_b32_e32 v77, 0xffff0000, v58
	v_lshlrev_b32_e32 v58, 16, v59
	v_and_b32_e32 v59, 0xffff0000, v59
	v_add_f32_e32 v62, v64, v56
	s_waitcnt vmcnt(13)
	v_lshlrev_b32_e32 v56, 16, v38
	v_and_b32_e32 v57, 0xffff0000, v38
	v_lshlrev_b32_e32 v38, 16, v39
	v_and_b32_e32 v39, 0xffff0000, v39
	s_waitcnt vmcnt(12)
	v_lshlrev_b32_e32 v60, 16, v36
	v_and_b32_e32 v61, 0xffff0000, v36
	v_lshlrev_b32_e32 v36, 16, v37
	v_and_b32_e32 v37, 0xffff0000, v37
	v_pk_fma_f32 v[56:57], v[146:147], v[56:57], v[76:77] op_sel_hi:[0,1,1]
	v_pk_fma_f32 v[38:39], v[146:147], v[38:39], v[58:59] op_sel_hi:[0,1,1]
	v_pk_fma_f32 v[36:37], v[146:147], v[36:37], v[38:39] op_sel:[1,0,0]
	v_pk_fma_f32 v[16:17], v[146:147], v[60:61], v[56:57] op_sel:[1,0,0]
	v_mul_f32_e32 v39, v37, v37
	v_mul_f32_e32 v38, v17, v17
	v_fmac_f32_e32 v38, v16, v16
	v_fmac_f32_e32 v39, v36, v36
	v_add_f32_e32 v38, v38, v39
	v_add_f32_e32 v38, v62, v38
	s_andn2_b64 vcc, exec, s[24:25]
	s_waitcnt lgkmcnt(0)
	s_nop 1
	v_add_f32_dpp v38, v38, v38 quad_perm:[1,0,3,2] row_mask:0xf bank_mask:0xf
	s_waitcnt lgkmcnt(0)
	s_nop 1
	v_add_f32_dpp v38, v38, v38 quad_perm:[2,3,0,1] row_mask:0xf bank_mask:0xf
	s_waitcnt lgkmcnt(0)
	s_nop 1
	v_add_f32_dpp v38, v38, v38 row_half_mirror row_mask:0xf bank_mask:0xf
	s_waitcnt lgkmcnt(0)
	s_nop 1
	v_add_f32_dpp v38, v38, v38 row_mirror row_mask:0xf bank_mask:0xf
	v_mov_b32_e32 v39, v38
	s_waitcnt lgkmcnt(0)
	s_nop 1
	v_permlane16_swap_b32_e32 v39, v38
	v_add_f32_e32 v38, v38, v39
	v_mov_b32_e32 v39, v38
	s_nop 1
	v_permlane32_swap_b32_e32 v38, v39
	s_cbranch_vccnz .LBB0_1653
	v_add_f32_e32 v38, v38, v39
	s_and_b64 vcc, exec, s[6:7]
	s_mov_b64 s[10:11], -1
	s_cbranch_vccnz .LBB0_1651
	v_cvt_pk_bf16_f32 v56, v54, v55
	v_cvt_pk_bf16_f32 v57, v52, v53
	global_store_dwordx2 v[20:21], v[56:57], off
	v_cvt_pk_bf16_f32 v56, v50, v51
	v_cvt_pk_bf16_f32 v57, v48, v49
	global_store_dwordx2 v[20:21], v[56:57], off offset:512
	v_cvt_pk_bf16_f32 v56, v46, v47
	v_cvt_pk_bf16_f32 v57, v44, v45
	global_store_dwordx2 v[20:21], v[56:57], off offset:1024
	v_cvt_pk_bf16_f32 v56, v16, v17
	v_cvt_pk_bf16_f32 v57, v36, v37
	global_store_dwordx2 v[20:21], v[56:57], off offset:1536
	s_and_saveexec_b64 s[10:11], s[0:1]
	s_cbranch_execz .LBB0_1650
	s_lshl_b64 s[2:3], s[22:23], 6
	v_cndmask_b32_e64 v39, 0, v38, s[4:5]
	v_lshl_add_u64 v[20:21], v[0:1], 0, s[2:3]
	global_store_dword v[20:21], v39, off

; __device__ __forceinline__ float bf_lo(unsigned w) { return __uint_as_float(w << 16); }
; __device__ __forceinline__ float bf_hi(unsigned w) { return __uint_as_float(w & 0xffff0000u); }
; __device__ __forceinline__ float wave_sum(float v) { return half_sum(sum32(v)); }
; __device__ __forceinline__ void st_bf4(bf16_t* p, f32x4 v) { u32x2 w; w.x = cvt_pk_bf16(v[0], v[1]); w.y = cvt_pk_bf16(v[2], v[3]); *(u32x2*)p = w; }
; template <int NTK>
; __device__ __forceinline__ void combine_rows(int t0, int tstride, const LAS int* bst, const int* tok_e, const int* tok_pos, const float* tok_w, const bf16_t* Y, const bf16_t* xbi, float* xio, bf16_t* xb, float* part, const float* gfin, bool last, int lane) {
;     ...
;     for (int i = 0; i < NTK; ++i) { float s = 0.f;
; #pragma unroll
;         for (int j = 0; j < 4; ++j) { const f32x4 a = {bf_lo(ya[i][j].x), bf_hi(ya[i][j].x), bf_lo(ya[i][j].y), bf_hi(ya[i][j].y)}, b = {bf_lo(yb[i][j].x), bf_hi(yb[i][j].x), bf_lo(yb[i][j].y), bf_hi(yb[i][j].y)};
;             v[i][j] = v[i][j] + w0[i] * a + w1[i] * b;
;             s += (v[i][j][0] * v[i][j][0] + v[i][j][1] * v[i][j][1]) + (v[i][j][2] * v[i][j][2] + v[i][j][3] * v[i][j][3]); }
;         s = wave_sum(s);
;         if (ok[i]) { const int t = tk[i];
;             if (!last) {
; #pragma unroll
;                 for (int j = 0; j < 4; ++j) { const int c = j * 256 + lane * 4; st_bf4(xb + (size_t)t * DM + c, v[i][j]); }
;                 if (lane < 16) part[(size_t)t * 16 + lane] = lane == 0 ? s : 0.f;
.LBB0_1653:
	s_waitcnt vmcnt(11)
	v_lshlrev_b32_e32 v16, 16, v32
	v_and_b32_e32 v17, 0xffff0000, v32
	v_lshlrev_b32_e32 v20, 16, v33
	v_and_b32_e32 v21, 0xffff0000, v33
	s_waitcnt vmcnt(10)
	v_lshlrev_b32_e32 v32, 16, v30
	v_and_b32_e32 v33, 0xffff0000, v30
	v_lshlrev_b32_e32 v30, 16, v31
	v_and_b32_e32 v31, 0xffff0000, v31
	s_waitcnt vmcnt(9)
	v_lshlrev_b32_e32 v48, 16, v34
	v_and_b32_e32 v49, 0xffff0000, v34
	v_lshlrev_b32_e32 v34, 16, v35
	v_and_b32_e32 v35, 0xffff0000, v35
	v_pk_fma_f32 v[16:17], v[150:151], v[32:33], v[16:17] op_sel_hi:[0,1,1]
	v_pk_fma_f32 v[20:21], v[150:151], v[30:31], v[20:21] op_sel_hi:[0,1,1]
	v_pk_fma_f32 v[30:31], v[150:151], v[34:35], v[20:21] op_sel:[1,0,0]
	v_pk_fma_f32 v[32:33], v[150:151], v[48:49], v[16:17] op_sel:[1,0,0]
	v_mul_f32_e32 v17, v31, v31
	v_mul_f32_e32 v16, v33, v33
	v_fmac_f32_e32 v16, v32, v32
	v_fmac_f32_e32 v17, v30, v30
	s_waitcnt vmcnt(8)
	v_lshlrev_b32_e32 v36, 16, v40
	v_and_b32_e32 v37, 0xffff0000, v40
	v_lshlrev_b32_e32 v38, 16, v41
	v_and_b32_e32 v39, 0xffff0000, v41
	v_add_f32_e32 v48, v16, v17
	s_waitcnt vmcnt(7)
	v_lshlrev_b32_e32 v16, 16, v26
	v_and_b32_e32 v17, 0xffff0000, v26
	v_lshlrev_b32_e32 v20, 16, v27
	v_and_b32_e32 v21, 0xffff0000, v27
	s_waitcnt vmcnt(6)
	v_lshlrev_b32_e32 v26, 16, v28
	v_and_b32_e32 v27, 0xffff0000, v28
	v_lshlrev_b32_e32 v28, 16, v29
	v_and_b32_e32 v29, 0xffff0000, v29
	v_pk_fma_f32 v[34:35], v[150:151], v[16:17], v[36:37] op_sel_hi:[0,1,1]
	v_pk_fma_f32 v[16:17], v[150:151], v[20:21], v[38:39] op_sel_hi:[0,1,1]
	v_pk_fma_f32 v[16:17], v[150:151], v[28:29], v[16:17] op_sel:[1,0,0]
	v_pk_fma_f32 v[26:27], v[150:151], v[26:27], v[34:35] op_sel:[1,0,0]
	v_mul_f32_e32 v21, v17, v17
	v_mul_f32_e32 v20, v27, v27
	v_fmac_f32_e32 v20, v26, v26
	v_fmac_f32_e32 v21, v16, v16
	v_add_f32_e32 v20, v20, v21
	s_waitcnt vmcnt(5)
	v_lshlrev_b32_e32 v40, 16, v42
	v_and_b32_e32 v41, 0xffff0000, v42
	v_lshlrev_b32_e32 v42, 16, v43
	v_and_b32_e32 v43, 0xffff0000, v43
	v_add_f32_e32 v36, v48, v20
	s_waitcnt vmcnt(4)
	v_lshlrev_b32_e32 v20, 16, v22
	v_and_b32_e32 v21, 0xffff0000, v22
	v_lshlrev_b32_e32 v22, 16, v23
	v_and_b32_e32 v23, 0xffff0000, v23
	s_waitcnt vmcnt(3)
	v_lshlrev_b32_e32 v28, 16, v24
	v_and_b32_e32 v29, 0xffff0000, v24
	v_lshlrev_b32_e32 v24, 16, v25
	v_and_b32_e32 v25, 0xffff0000, v25
	v_pk_fma_f32 v[34:35], v[150:151], v[20:21], v[40:41] op_sel_hi:[0,1,1]
	v_pk_fma_f32 v[20:21], v[150:151], v[22:23], v[42:43] op_sel_hi:[0,1,1]
	v_pk_fma_f32 v[20:21], v[150:151], v[24:25], v[20:21] op_sel:[1,0,0]
	v_pk_fma_f32 v[24:25], v[150:151], v[28:29], v[34:35] op_sel:[1,0,0]
	v_mul_f32_e32 v23, v21, v21
	v_mul_f32_e32 v22, v25, v25
	v_fmac_f32_e32 v22, v24, v24
	v_fmac_f32_e32 v23, v20, v20
	v_add_f32_e32 v22, v22, v23
	s_waitcnt vmcnt(2)
	v_lshlrev_b32_e32 v44, 16, v70
	v_and_b32_e32 v45, 0xffff0000, v70
	v_lshlrev_b32_e32 v46, 16, v71
	v_and_b32_e32 v47, 0xffff0000, v71
	v_add_f32_e32 v40, v36, v22
	s_waitcnt vmcnt(1)
	v_lshlrev_b32_e32 v22, 16, v66
	v_and_b32_e32 v23, 0xffff0000, v66
	v_lshlrev_b32_e32 v28, 16, v67
	v_and_b32_e32 v29, 0xffff0000, v67
	s_waitcnt vmcnt(0)
	v_lshlrev_b32_e32 v34, 16, v68
	v_and_b32_e32 v35, 0xffff0000, v68
	v_lshlrev_b32_e32 v36, 16, v69
	v_and_b32_e32 v37, 0xffff0000, v69
	v_pk_fma_f32 v[38:39], v[150:151], v[22:23], v[44:45] op_sel_hi:[0,1,1]
	v_pk_fma_f32 v[22:23], v[150:151], v[28:29], v[46:47] op_sel_hi:[0,1,1]
	v_pk_fma_f32 v[22:23], v[150:151], v[36:37], v[22:23] op_sel:[1,0,0]
	v_pk_fma_f32 v[14:15], v[150:151], v[34:35], v[38:39] op_sel:[1,0,0]
	v_mul_f32_e32 v29, v23, v23
	v_mul_f32_e32 v28, v15, v15
	v_fmac_f32_e32 v28, v14, v14
	v_fmac_f32_e32 v29, v22, v22
	v_add_f32_e32 v28, v28, v29
	v_add_f32_e32 v28, v40, v28
	s_andn2_b64 vcc, exec, s[20:21]
	s_waitcnt lgkmcnt(0)
	s_nop 1
	v_add_f32_dpp v28, v28, v28 quad_perm:[1,0,3,2] row_mask:0xf bank_mask:0xf
	s_waitcnt lgkmcnt(0)
	s_nop 1
	v_add_f32_dpp v28, v28, v28 quad_perm:[2,3,0,1] row_mask:0xf bank_mask:0xf
	s_waitcnt lgkmcnt(0)
	s_nop 1
	v_add_f32_dpp v28, v28, v28 row_half_mirror row_mask:0xf bank_mask:0xf
	s_waitcnt lgkmcnt(0)
	s_nop 1
	v_add_f32_dpp v28, v28, v28 row_mirror row_mask:0xf bank_mask:0xf
	v_mov_b32_e32 v29, v28
	s_waitcnt lgkmcnt(0)
	s_nop 1
	v_permlane16_swap_b32_e32 v29, v28
	v_add_f32_e32 v28, v28, v29
	v_mov_b32_e32 v29, v28
	s_nop 1
	v_permlane32_swap_b32_e32 v28, v29
	s_cbranch_vccnz .LBB0_1632
	v_add_f32_e32 v28, v28, v29
	s_and_b64 vcc, exec, s[6:7]
	s_mov_b64 s[6:7], -1
	s_cbranch_vccnz .LBB0_1658
	v_cvt_pk_bf16_f32 v34, v32, v33
	v_cvt_pk_bf16_f32 v35, v30, v31
	global_store_dwordx2 v[18:19], v[34:35], off
	v_cvt_pk_bf16_f32 v34, v26, v27
	v_cvt_pk_bf16_f32 v35, v16, v17
	global_store_dwordx2 v[18:19], v[34:35], off offset:512
	v_cvt_pk_bf16_f32 v34, v24, v25
	v_cvt_pk_bf16_f32 v35, v20, v21
	global_store_dwordx2 v[18:19], v[34:35], off offset:1024
	v_cvt_pk_bf16_f32 v34, v14, v15
	v_cvt_pk_bf16_f32 v35, v22, v23
	global_store_dwordx2 v[18:19], v[34:35], off offset:1536
	s_and_saveexec_b64 s[6:7], s[0:1]
	s_cbranch_execz .LBB0_1657
	s_lshl_b64 s[2:3], s[18:19], 6
	v_cndmask_b32_e64 v29, 0, v28, s[4:5]
	v_lshl_add_u64 v[18:19], v[0:1], 0, s[2:3]
	global_store_dword v[18:19], v29, off
